# v31 + barrier leaders no longer bump the unused per-XCD generation word (atomic + ack wait off the leader exit path, now exposed since the invalidate moved)
# baseline (speedup 1.0000x reference)
.LBB0_123:
	s_or_b64 exec, exec, s[6:7]
	s_mov_b64 s[6:7], exec
	v_mbcnt_lo_u32_b32 v1, s6, 0
	v_mbcnt_hi_u32_b32 v1, s7, v1
	v_cmp_eq_u32_e32 vcc, 0, v1
	s_waitcnt vmcnt(0)
	s_and_saveexec_b64 s[8:9], vcc
	s_cbranch_execz .LBB0_125
	s_bcnt1_i32_b64 s6, s[6:7]
	v_mov_b32_e32 v1, 0x2000
	v_mov_b32_e32 v2, s6
.LBB0_125:
	s_or_b64 exec, exec, s[8:9]
	s_waitcnt vmcnt(0)

.LBB0_186:
	s_or_b64 exec, exec, s[6:7]
	s_mov_b64 s[6:7], exec
	v_mbcnt_lo_u32_b32 v1, s6, 0
	v_mbcnt_hi_u32_b32 v1, s7, v1
	v_cmp_eq_u32_e32 vcc, 0, v1
	s_waitcnt vmcnt(0)
	s_and_saveexec_b64 s[8:9], vcc
	s_cbranch_execz .LBB0_188
	s_bcnt1_i32_b64 s6, s[6:7]
	v_mov_b32_e32 v1, 0x2000
	v_mov_b32_e32 v2, s6
.LBB0_188:
	s_or_b64 exec, exec, s[8:9]
	s_waitcnt vmcnt(0)

.LBB0_673:
	s_or_b64 exec, exec, s[6:7]
	s_mov_b64 s[6:7], exec
	v_mbcnt_lo_u32_b32 v1, s6, 0
	v_mbcnt_hi_u32_b32 v1, s7, v1
	v_cmp_eq_u32_e32 vcc, 0, v1
	s_waitcnt vmcnt(0)
	s_and_saveexec_b64 s[8:9], vcc
	s_cbranch_execz .LBB0_675
	s_bcnt1_i32_b64 s6, s[6:7]
	v_mov_b32_e32 v1, 0x2000
	v_mov_b32_e32 v2, s6
.LBB0_675:
	s_or_b64 exec, exec, s[8:9]
	s_waitcnt vmcnt(0)

.LBB0_863:
	s_or_b64 exec, exec, s[6:7]
	s_mov_b64 s[6:7], exec
	v_mbcnt_lo_u32_b32 v1, s6, 0
	v_mbcnt_hi_u32_b32 v1, s7, v1
	v_cmp_eq_u32_e32 vcc, 0, v1
	s_waitcnt vmcnt(0)
	s_and_saveexec_b64 s[8:9], vcc
	s_cbranch_execz .LBB0_865
	s_bcnt1_i32_b64 s6, s[6:7]
	v_mov_b32_e32 v1, 0x2000
	v_mov_b32_e32 v2, s6
.LBB0_865:
	s_or_b64 exec, exec, s[8:9]
	s_waitcnt vmcnt(0)

.LBB0_928:
	s_or_b64 exec, exec, s[6:7]
	s_mov_b64 s[6:7], exec
	v_mbcnt_lo_u32_b32 v1, s6, 0
	v_mbcnt_hi_u32_b32 v1, s7, v1
	v_cmp_eq_u32_e32 vcc, 0, v1
	s_waitcnt vmcnt(0)
	s_and_saveexec_b64 s[8:9], vcc
	s_cbranch_execz .LBB0_930
	s_bcnt1_i32_b64 s6, s[6:7]
	v_mov_b32_e32 v1, 0x2000
	v_mov_b32_e32 v2, s6
.LBB0_930:
	s_or_b64 exec, exec, s[8:9]
	s_waitcnt vmcnt(0)

.LBB0_1036:
	s_or_b64 exec, exec, s[6:7]
	s_mov_b64 s[6:7], exec
	v_mbcnt_lo_u32_b32 v1, s6, 0
	v_mbcnt_hi_u32_b32 v1, s7, v1
	v_cmp_eq_u32_e32 vcc, 0, v1
	s_waitcnt vmcnt(0)
	s_and_saveexec_b64 s[8:9], vcc
	s_cbranch_execz .LBB0_1038
	s_bcnt1_i32_b64 s6, s[6:7]
	v_mov_b32_e32 v1, 0x2000
	v_mov_b32_e32 v2, s6
.LBB0_1038:
	s_or_b64 exec, exec, s[8:9]
	s_waitcnt vmcnt(0)

.LBB0_1120:
	s_or_b64 exec, exec, s[6:7]
	s_mov_b64 s[6:7], exec
	v_mbcnt_lo_u32_b32 v1, s6, 0
	v_mbcnt_hi_u32_b32 v1, s7, v1
	v_cmp_eq_u32_e32 vcc, 0, v1
	s_waitcnt vmcnt(0)
	s_and_saveexec_b64 s[8:9], vcc
	s_cbranch_execz .LBB0_1122
	s_bcnt1_i32_b64 s6, s[6:7]
	v_mov_b32_e32 v1, 0x2000
	v_mov_b32_e32 v2, s6
.LBB0_1122:
	s_or_b64 exec, exec, s[8:9]
	s_waitcnt vmcnt(0)

.LBB0_1204:
	s_or_b64 exec, exec, s[6:7]
	s_mov_b64 s[6:7], exec
	v_mbcnt_lo_u32_b32 v1, s6, 0
	v_mbcnt_hi_u32_b32 v1, s7, v1
	v_cmp_eq_u32_e32 vcc, 0, v1
	s_waitcnt vmcnt(0)
	s_and_saveexec_b64 s[8:9], vcc
	s_cbranch_execz .LBB0_1206
	s_bcnt1_i32_b64 s6, s[6:7]
	v_mov_b32_e32 v1, 0x2000
	v_mov_b32_e32 v2, s6
.LBB0_1206:
	s_or_b64 exec, exec, s[8:9]
	s_waitcnt vmcnt(0)

.LBB0_1508:
	s_or_b64 exec, exec, s[6:7]
	s_mov_b64 s[6:7], exec
	v_mbcnt_lo_u32_b32 v1, s6, 0
	v_mbcnt_hi_u32_b32 v1, s7, v1
	v_cmp_eq_u32_e32 vcc, 0, v1
	s_waitcnt vmcnt(0)
	s_and_saveexec_b64 s[8:9], vcc
	s_cbranch_execz .LBB0_1510
	s_bcnt1_i32_b64 s6, s[6:7]
	v_mov_b32_e32 v1, 0x2000
	v_mov_b32_e32 v2, s6
.LBB0_1510:
	s_or_b64 exec, exec, s[8:9]
	s_waitcnt vmcnt(0)

.LBB0_1588:
	s_or_b64 exec, exec, s[6:7]
	s_mov_b64 s[6:7], exec
	v_mbcnt_lo_u32_b32 v1, s6, 0
	v_mbcnt_hi_u32_b32 v1, s7, v1
	v_cmp_eq_u32_e32 vcc, 0, v1
	s_waitcnt vmcnt(0)
	s_and_saveexec_b64 s[8:9], vcc
	s_cbranch_execz .LBB0_1590
	s_bcnt1_i32_b64 s6, s[6:7]
	v_mov_b32_e32 v1, 0x2000
	v_mov_b32_e32 v2, s6
.LBB0_1590:
	s_or_b64 exec, exec, s[8:9]
	s_waitcnt vmcnt(0)

.LBB0_1908:
	s_or_b64 exec, exec, s[6:7]
	s_mov_b64 s[6:7], exec
	v_mbcnt_lo_u32_b32 v1, s6, 0
	v_mbcnt_hi_u32_b32 v1, s7, v1
	v_cmp_eq_u32_e32 vcc, 0, v1
	s_waitcnt vmcnt(0)
	s_and_saveexec_b64 s[8:9], vcc
	s_cbranch_execz .LBB0_1910
	s_bcnt1_i32_b64 s6, s[6:7]
	v_mov_b32_e32 v1, 0x2000
	v_mov_b32_e32 v2, s6
.LBB0_1910:
	s_or_b64 exec, exec, s[8:9]
	s_waitcnt vmcnt(0)

.LBB0_2056:
	s_or_b64 exec, exec, s[6:7]
	s_mov_b64 s[6:7], exec
	v_mbcnt_lo_u32_b32 v0, s6, 0
	v_mbcnt_hi_u32_b32 v0, s7, v0
	v_cmp_eq_u32_e32 vcc, 0, v0
	s_waitcnt vmcnt(0)
	s_and_saveexec_b64 s[8:9], vcc
	s_cbranch_execz .LBB0_2058
	s_bcnt1_i32_b64 s6, s[6:7]
	v_mov_b32_e32 v0, 0x2000
	v_mov_b32_e32 v1, s6
.LBB0_2058:
	s_or_b64 exec, exec, s[8:9]
	s_waitcnt vmcnt(0)
